# speedup vs baseline: 1.0084x; 1.0084x over previous
_Z12score_kernelPKfP15HIP_vector_typeIjLj2EES0_S0_:
	s_load_dwordx4 s[4:7], s[0:1], 0x0
	s_load_dwordx4 s[32:35], s[0:1], 0x10
	s_and_b32 s15, s2, 7
	s_lshl_b32 s15, s15, 2
	s_lshr_b32 s17, s2, 6
	s_add_u32 s15, s15, s17
	s_bfe_u32 s16, s2, 0x30003
	s_mul_i32 s17, s16, 0x271
	v_add_u32_e32 v2, s17, v0
	v_lshlrev_b32_e32 v1, 2, v2
	s_movk_i32 s17, 0x271
	v_cmp_gt_u32_e32 vcc, s17, v0
	v_readfirstlane_b32 s21, v0
	s_and_b64 exec, exec, vcc
	s_mov_b64 s[18:19], exec
	s_lshr_b32 s21, s21, 6
	s_movk_i32 s13, 0x4e20
	s_mov_b32 s14, 0x3fb8aa3b
	s_mov_b32 s12, 0
	s_mov_b32 s10, 0x13d620
	s_mov_b32 s11, 0x20000
	s_mul_i32 s17, s15, 0x13d620
	s_mul_hi_u32 s20, s15, 0x13d620
	s_mov_b32 s40, 0
	s_add_u32 s41, s40, s13
	s_add_u32 s42, s41, s13
	s_add_u32 s43, s42, s13
	s_add_u32 s44, s43, s13
	s_add_u32 s45, s44, s13
	s_add_u32 s46, s45, s13
	s_add_u32 s47, s46, s13
	s_add_u32 s48, s47, s13
	s_add_u32 s49, s48, s13
	s_add_u32 s50, s49, s13
	s_add_u32 s51, s50, s13
	s_add_u32 s52, s51, s13
	s_add_u32 s53, s52, s13
	s_add_u32 s54, s53, s13
	s_add_u32 s55, s54, s13
	s_cmp_lg_u32 s21, 0
	s_cbranch_scc1 .Lk1_nowarm0
	s_getpc_b64 s[30:31]
	v_lshlrev_b32_e32 v3, 6, v0
	global_load_dword v92, v3, s[30:31]
	s_add_u32 s30, s30, 0x1000
	s_addc_u32 s31, s31, 0
	global_load_dword v93, v3, s[30:31]
	s_add_u32 s30, s30, 0x1000
	s_addc_u32 s31, s31, 0
	global_load_dword v94, v3, s[30:31]
	s_and_b32 s30, s0, 0xfffff000
	s_mov_b32 s31, s1
	global_load_dword v95, v3, s[30:31]

.Lk1_nowarm9:
	buffer_load_dword v8, v1, s[8:11], s40 offen nt
	buffer_load_dword v9, v1, s[8:11], s41 offen nt
	buffer_load_dword v10, v1, s[8:11], s42 offen nt
	buffer_load_dword v11, v1, s[8:11], s43 offen nt
	buffer_load_dword v12, v1, s[8:11], s44 offen nt
	buffer_load_dword v13, v1, s[8:11], s45 offen nt
	buffer_load_dword v14, v1, s[8:11], s46 offen nt
	buffer_load_dword v15, v1, s[8:11], s47 offen nt
	buffer_load_dword v16, v1, s[8:11], s48 offen nt
	buffer_load_dword v17, v1, s[8:11], s49 offen nt
	buffer_load_dword v18, v1, s[8:11], s50 offen nt
	buffer_load_dword v19, v1, s[8:11], s51 offen nt
	buffer_load_dword v20, v1, s[8:11], s52 offen nt
	buffer_load_dword v21, v1, s[8:11], s53 offen nt
	buffer_load_dword v22, v1, s[8:11], s54 offen nt
	buffer_load_dword v23, v1, s[8:11], s55 offen nt
	s_add_u32 s8, s8, 0x4e200
	s_addc_u32 s9, s9, 0
	buffer_load_dword v24, v1, s[8:11], s40 offen nt
	buffer_load_dword v25, v1, s[8:11], s41 offen nt
	buffer_load_dword v26, v1, s[8:11], s42 offen nt
	buffer_load_dword v27, v1, s[8:11], s43 offen nt
	buffer_load_dword v28, v1, s[8:11], s44 offen nt
	buffer_load_dword v29, v1, s[8:11], s45 offen nt
	buffer_load_dword v30, v1, s[8:11], s46 offen nt
	buffer_load_dword v31, v1, s[8:11], s47 offen nt
	buffer_load_dword v32, v1, s[8:11], s48 offen nt
	buffer_load_dword v33, v1, s[8:11], s49 offen nt
	buffer_load_dword v34, v1, s[8:11], s50 offen nt
	buffer_load_dword v35, v1, s[8:11], s51 offen nt
	buffer_load_dword v36, v1, s[8:11], s52 offen nt
	buffer_load_dword v37, v1, s[8:11], s53 offen nt
	buffer_load_dword v38, v1, s[8:11], s54 offen nt
	buffer_load_dword v39, v1, s[8:11], s55 offen nt
	s_add_u32 s8, s8, 0x4e200
	s_addc_u32 s9, s9, 0
	buffer_load_dword v40, v1, s[8:11], s40 offen nt
	buffer_load_dword v41, v1, s[8:11], s41 offen nt
	buffer_load_dword v42, v1, s[8:11], s42 offen nt
	buffer_load_dword v43, v1, s[8:11], s43 offen nt
	buffer_load_dword v44, v1, s[8:11], s44 offen nt
	buffer_load_dword v45, v1, s[8:11], s45 offen nt
	buffer_load_dword v46, v1, s[8:11], s46 offen nt
	buffer_load_dword v47, v1, s[8:11], s47 offen nt
	buffer_load_dword v48, v1, s[8:11], s48 offen nt
	buffer_load_dword v49, v1, s[8:11], s49 offen nt
	buffer_load_dword v50, v1, s[8:11], s50 offen nt
	buffer_load_dword v51, v1, s[8:11], s51 offen nt
	buffer_load_dword v52, v1, s[8:11], s52 offen nt
	buffer_load_dword v53, v1, s[8:11], s53 offen nt
	buffer_load_dword v54, v1, s[8:11], s54 offen nt
	buffer_load_dword v55, v1, s[8:11], s55 offen nt
	v_mul_u32_u24_e32 v3, 0x147b, v2
	v_lshrrev_b32_e32 v3, 19, v3
	v_mul_u32_u24_e32 v98, 0x64, v3
	v_sub_u32_e32 v98, v2, v98
	v_add_u32_e32 v3, -1, v3
	v_add_u32_e32 v98, -1, v98
	s_movk_i32 s17, 0x62
	v_cmp_gt_u32_e64 s[36:37], 48, v3
	v_cmp_gt_u32_e64 s[38:39], s17, v98
	s_mul_i32 s17, s15, 0x1388
	v_add_lshl_u32 v98, v2, s17, 3
	s_and_b64 s[36:37], s[36:37], s[38:39]
	s_waitcnt vmcnt(32)
	v_max3_f32 v76, v8, v9, v10
	v_max3_f32 v76, v76, v11, v12
	v_max3_f32 v76, v76, v13, v14
	v_max3_f32 v76, v76, v15, v16
	v_max3_f32 v76, v76, v17, v18
	v_max3_f32 v76, v76, v19, v20
	v_max3_f32 v76, v76, v21, v22
	v_max_f32_e32 v76, v76, v23
	v_sub_f32_e32 v8, v8, v76
	v_sub_f32_e32 v9, v9, v76
	v_sub_f32_e32 v10, v10, v76
	v_sub_f32_e32 v11, v11, v76
	v_sub_f32_e32 v12, v12, v76
	v_sub_f32_e32 v13, v13, v76
	v_sub_f32_e32 v14, v14, v76
	v_sub_f32_e32 v15, v15, v76
	v_sub_f32_e32 v16, v16, v76
	v_sub_f32_e32 v17, v17, v76
	v_sub_f32_e32 v18, v18, v76
	v_sub_f32_e32 v19, v19, v76
	v_sub_f32_e32 v20, v20, v76
	v_sub_f32_e32 v21, v21, v76
	v_sub_f32_e32 v22, v22, v76
	v_sub_f32_e32 v23, v23, v76
	v_or_b32_e32 v81, 0, v8
	v_or_b32_e32 v82, 1, v9
	v_min_u32_e32 v80, v81, v82
	v_or_b32_e32 v81, 2, v10
	v_or_b32_e32 v82, 3, v11
	v_min3_u32 v80, v80, v81, v82
	v_or_b32_e32 v81, 4, v12
	v_or_b32_e32 v82, 5, v13
	v_min3_u32 v80, v80, v81, v82
	v_or_b32_e32 v81, 6, v14
	v_or_b32_e32 v82, 7, v15
	v_min3_u32 v80, v80, v81, v82
	v_or_b32_e32 v81, 8, v16
	v_or_b32_e32 v82, 9, v17
	v_min3_u32 v80, v80, v81, v82
	v_or_b32_e32 v81, 10, v18
	v_or_b32_e32 v82, 11, v19
	v_min3_u32 v80, v80, v81, v82
	v_or_b32_e32 v81, 12, v20
	v_or_b32_e32 v82, 13, v21
	v_min3_u32 v80, v80, v81, v82
	v_or_b32_e32 v81, 14, v22
	v_or_b32_e32 v82, 15, v23
	v_min3_u32 v80, v80, v81, v82
	v_mul_f32_e32 v8, s14, v8
	v_mul_f32_e32 v9, s14, v9
	v_mul_f32_e32 v10, s14, v10
	v_mul_f32_e32 v11, s14, v11
	v_mul_f32_e32 v12, s14, v12
	v_mul_f32_e32 v13, s14, v13
	v_mul_f32_e32 v14, s14, v14
	v_mul_f32_e32 v15, s14, v15
	v_mul_f32_e32 v16, s14, v16
	v_mul_f32_e32 v17, s14, v17
	v_mul_f32_e32 v18, s14, v18
	v_mul_f32_e32 v19, s14, v19
	v_mul_f32_e32 v20, s14, v20
	v_mul_f32_e32 v21, s14, v21
	v_mul_f32_e32 v22, s14, v22
	v_mul_f32_e32 v23, s14, v23
	v_exp_f32_e32 v8, v8
	v_exp_f32_e32 v9, v9
	v_exp_f32_e32 v10, v10
	v_exp_f32_e32 v11, v11
	v_exp_f32_e32 v12, v12
	v_exp_f32_e32 v13, v13
	v_exp_f32_e32 v14, v14
	v_exp_f32_e32 v15, v15
	v_exp_f32_e32 v16, v16
	v_exp_f32_e32 v17, v17
	v_exp_f32_e32 v18, v18
	v_exp_f32_e32 v19, v19
	v_exp_f32_e32 v20, v20
	v_exp_f32_e32 v21, v21
	v_exp_f32_e32 v22, v22
	v_exp_f32_e32 v23, v23
	v_add_f32_e32 v78, v8, v10
	v_add_f32_e32 v79, v9, v11
	v_add_f32_e32 v78, v78, v12
	v_add_f32_e32 v79, v79, v13
	v_add_f32_e32 v78, v78, v14
	v_add_f32_e32 v79, v79, v15
	v_add_f32_e32 v78, v78, v16
	v_add_f32_e32 v79, v79, v17
	v_add_f32_e32 v78, v78, v18
	v_add_f32_e32 v79, v79, v19
	v_add_f32_e32 v78, v78, v20
	v_add_f32_e32 v79, v79, v21
	v_add_f32_e32 v78, v78, v22
	v_add_f32_e32 v79, v79, v23
	v_add_f32_e32 v78, v78, v79
	v_cvt_f64_f32_e32 v[86:87], v78
	v_mov_b32_e32 v75, v80
	v_mov_b32_e32 v73, v76
	s_add_u32 s8, s8, 0x4e200
	s_addc_u32 s9, s9, 0
	buffer_load_dword v56, v1, s[8:11], s40 offen nt
	buffer_load_dword v57, v1, s[8:11], s41 offen nt
	buffer_load_dword v58, v1, s[8:11], s42 offen nt
	buffer_load_dword v59, v1, s[8:11], s43 offen nt
	buffer_load_dword v60, v1, s[8:11], s44 offen nt
	buffer_load_dword v61, v1, s[8:11], s45 offen nt
	buffer_load_dword v62, v1, s[8:11], s46 offen nt
	buffer_load_dword v63, v1, s[8:11], s47 offen nt
	buffer_load_dword v64, v1, s[8:11], s48 offen nt
	buffer_load_dword v65, v1, s[8:11], s49 offen nt
	buffer_load_dword v66, v1, s[8:11], s50 offen nt
	buffer_load_dword v67, v1, s[8:11], s51 offen nt
	buffer_load_dword v68, v1, s[8:11], s52 offen nt
	buffer_load_dword v69, v1, s[8:11], s53 offen nt
	buffer_load_dword v70, v1, s[8:11], s54 offen nt
	buffer_load_dword v71, v1, s[8:11], s55 offen nt
	s_add_u32 s8, s8, 0x4e200
	s_addc_u32 s9, s9, 0
	buffer_load_dword v72, v1, s[8:11], s40 offen nt
	s_waitcnt vmcnt(33)
	v_max3_f32 v76, v24, v25, v26
	v_max3_f32 v76, v76, v27, v28
	v_max3_f32 v76, v76, v29, v30
	v_max3_f32 v76, v76, v31, v32
	v_max3_f32 v76, v76, v33, v34
	v_max3_f32 v76, v76, v35, v36
	v_max3_f32 v76, v76, v37, v38
	v_max_f32_e32 v76, v76, v39
	v_max_f32_e32 v77, v73, v76
	v_cmp_gt_f32_e64 s[20:21], v76, v73
	v_sub_f32_e32 v83, v73, v77
	v_mul_f32_e32 v83, s14, v83
	v_exp_f32_e32 v83, v83
	v_sub_f32_e32 v24, v24, v77
	v_sub_f32_e32 v25, v25, v77
	v_sub_f32_e32 v26, v26, v77
	v_sub_f32_e32 v27, v27, v77
	v_sub_f32_e32 v28, v28, v77
	v_sub_f32_e32 v29, v29, v77
	v_sub_f32_e32 v30, v30, v77
	v_sub_f32_e32 v31, v31, v77
	v_sub_f32_e32 v32, v32, v77
	v_sub_f32_e32 v33, v33, v77
	v_sub_f32_e32 v34, v34, v77
	v_sub_f32_e32 v35, v35, v77
	v_sub_f32_e32 v36, v36, v77
	v_sub_f32_e32 v37, v37, v77
	v_sub_f32_e32 v38, v38, v77
	v_sub_f32_e32 v39, v39, v77
	v_cvt_f64_f32_e32 v[84:85], v83
	v_or_b32_e32 v81, 16, v24
	v_or_b32_e32 v82, 17, v25
	v_min_u32_e32 v80, v81, v82
	v_or_b32_e32 v81, 18, v26
	v_or_b32_e32 v82, 19, v27
	v_min3_u32 v80, v80, v81, v82
	v_or_b32_e32 v81, 20, v28
	v_or_b32_e32 v82, 21, v29
	v_min3_u32 v80, v80, v81, v82
	v_or_b32_e32 v81, 22, v30
	v_or_b32_e32 v82, 23, v31
	v_min3_u32 v80, v80, v81, v82
	v_or_b32_e32 v81, 24, v32
	v_or_b32_e32 v82, 25, v33
	v_min3_u32 v80, v80, v81, v82
	v_or_b32_e32 v81, 26, v34
	v_or_b32_e32 v82, 27, v35
	v_min3_u32 v80, v80, v81, v82
	v_or_b32_e32 v81, 28, v36
	v_or_b32_e32 v82, 29, v37
	v_min3_u32 v80, v80, v81, v82
	v_or_b32_e32 v81, 30, v38
	v_or_b32_e32 v82, 31, v39
	v_min3_u32 v80, v80, v81, v82
	v_mul_f64 v[86:87], v[86:87], v[84:85]
	v_mul_f32_e32 v24, s14, v24
	v_mul_f32_e32 v25, s14, v25
	v_mul_f32_e32 v26, s14, v26
	v_mul_f32_e32 v27, s14, v27
	v_mul_f32_e32 v28, s14, v28
	v_mul_f32_e32 v29, s14, v29
	v_mul_f32_e32 v30, s14, v30
	v_mul_f32_e32 v31, s14, v31
	v_mul_f32_e32 v32, s14, v32
	v_mul_f32_e32 v33, s14, v33
	v_mul_f32_e32 v34, s14, v34
	v_mul_f32_e32 v35, s14, v35
	v_mul_f32_e32 v36, s14, v36
	v_mul_f32_e32 v37, s14, v37
	v_mul_f32_e32 v38, s14, v38
	v_mul_f32_e32 v39, s14, v39
	v_exp_f32_e32 v24, v24
	v_exp_f32_e32 v25, v25
	v_exp_f32_e32 v26, v26
	v_exp_f32_e32 v27, v27
	v_exp_f32_e32 v28, v28
	v_exp_f32_e32 v29, v29
	v_exp_f32_e32 v30, v30
	v_exp_f32_e32 v31, v31
	v_exp_f32_e32 v32, v32
	v_exp_f32_e32 v33, v33
	v_exp_f32_e32 v34, v34
	v_exp_f32_e32 v35, v35
	v_exp_f32_e32 v36, v36
	v_exp_f32_e32 v37, v37
	v_exp_f32_e32 v38, v38
	v_exp_f32_e32 v39, v39
	v_add_f32_e32 v78, v24, v26
	v_add_f32_e32 v79, v25, v27
	v_add_f32_e32 v78, v78, v28
	v_add_f32_e32 v79, v79, v29
	v_add_f32_e32 v78, v78, v30
	v_add_f32_e32 v79, v79, v31
	v_add_f32_e32 v78, v78, v32
	v_add_f32_e32 v79, v79, v33
	v_add_f32_e32 v78, v78, v34
	v_add_f32_e32 v79, v79, v35
	v_add_f32_e32 v78, v78, v36
	v_add_f32_e32 v79, v79, v37
	v_add_f32_e32 v78, v78, v38
	v_add_f32_e32 v79, v79, v39
	v_add_f32_e32 v78, v78, v79
	v_cvt_f64_f32_e32 v[84:85], v78
	v_cndmask_b32_e64 v75, v75, v80, s[20:21]
	v_mov_b32_e32 v73, v77
	v_add_f64 v[86:87], v[86:87], v[84:85]
	s_waitcnt vmcnt(17)
	v_max3_f32 v76, v40, v41, v42
	v_max3_f32 v76, v76, v43, v44
	v_max3_f32 v76, v76, v45, v46
	v_max3_f32 v76, v76, v47, v48
	v_max3_f32 v76, v76, v49, v50
	v_max3_f32 v76, v76, v51, v52
	v_max3_f32 v76, v76, v53, v54
	v_max_f32_e32 v76, v76, v55
	v_max_f32_e32 v77, v73, v76
	v_cmp_gt_f32_e64 s[20:21], v76, v73
	v_sub_f32_e32 v83, v73, v77
	v_mul_f32_e32 v83, s14, v83
	v_exp_f32_e32 v83, v83
	v_sub_f32_e32 v40, v40, v77
	v_sub_f32_e32 v41, v41, v77
	v_sub_f32_e32 v42, v42, v77
	v_sub_f32_e32 v43, v43, v77
	v_sub_f32_e32 v44, v44, v77
	v_sub_f32_e32 v45, v45, v77
	v_sub_f32_e32 v46, v46, v77
	v_sub_f32_e32 v47, v47, v77
	v_sub_f32_e32 v48, v48, v77
	v_sub_f32_e32 v49, v49, v77
	v_sub_f32_e32 v50, v50, v77
	v_sub_f32_e32 v51, v51, v77
	v_sub_f32_e32 v52, v52, v77
	v_sub_f32_e32 v53, v53, v77
	v_sub_f32_e32 v54, v54, v77
	v_sub_f32_e32 v55, v55, v77
	v_cvt_f64_f32_e32 v[84:85], v83
	v_or_b32_e32 v81, 32, v40
	v_or_b32_e32 v82, 33, v41
	v_min_u32_e32 v80, v81, v82
	v_or_b32_e32 v81, 34, v42
	v_or_b32_e32 v82, 35, v43
	v_min3_u32 v80, v80, v81, v82
	v_or_b32_e32 v81, 36, v44
	v_or_b32_e32 v82, 37, v45
	v_min3_u32 v80, v80, v81, v82
	v_or_b32_e32 v81, 38, v46
	v_or_b32_e32 v82, 39, v47
	v_min3_u32 v80, v80, v81, v82
	v_or_b32_e32 v81, 40, v48
	v_or_b32_e32 v82, 41, v49
	v_min3_u32 v80, v80, v81, v82
	v_or_b32_e32 v81, 42, v50
	v_or_b32_e32 v82, 43, v51
	v_min3_u32 v80, v80, v81, v82
	v_or_b32_e32 v81, 44, v52
	v_or_b32_e32 v82, 45, v53
	v_min3_u32 v80, v80, v81, v82
	v_or_b32_e32 v81, 46, v54
	v_or_b32_e32 v82, 47, v55
	v_min3_u32 v80, v80, v81, v82
	v_mul_f64 v[86:87], v[86:87], v[84:85]
	v_mul_f32_e32 v40, s14, v40
	v_mul_f32_e32 v41, s14, v41
	v_mul_f32_e32 v42, s14, v42
	v_mul_f32_e32 v43, s14, v43
	v_mul_f32_e32 v44, s14, v44
	v_mul_f32_e32 v45, s14, v45
	v_mul_f32_e32 v46, s14, v46
	v_mul_f32_e32 v47, s14, v47
	v_mul_f32_e32 v48, s14, v48
	v_mul_f32_e32 v49, s14, v49
	v_mul_f32_e32 v50, s14, v50
	v_mul_f32_e32 v51, s14, v51
	v_mul_f32_e32 v52, s14, v52
	v_mul_f32_e32 v53, s14, v53
	v_mul_f32_e32 v54, s14, v54
	v_mul_f32_e32 v55, s14, v55
	v_exp_f32_e32 v40, v40
	v_exp_f32_e32 v41, v41
	v_exp_f32_e32 v42, v42
	v_exp_f32_e32 v43, v43
	v_exp_f32_e32 v44, v44
	v_exp_f32_e32 v45, v45
	v_exp_f32_e32 v46, v46
	v_exp_f32_e32 v47, v47
	v_exp_f32_e32 v48, v48
	v_exp_f32_e32 v49, v49
	v_exp_f32_e32 v50, v50
	v_exp_f32_e32 v51, v51
	v_exp_f32_e32 v52, v52
	v_exp_f32_e32 v53, v53
	v_exp_f32_e32 v54, v54
	v_exp_f32_e32 v55, v55
	v_add_f32_e32 v78, v40, v42
	v_add_f32_e32 v79, v41, v43
	v_add_f32_e32 v78, v78, v44
	v_add_f32_e32 v79, v79, v45
	v_add_f32_e32 v78, v78, v46
	v_add_f32_e32 v79, v79, v47
	v_add_f32_e32 v78, v78, v48
	v_add_f32_e32 v79, v79, v49
	v_add_f32_e32 v78, v78, v50
	v_add_f32_e32 v79, v79, v51
	v_add_f32_e32 v78, v78, v52
	v_add_f32_e32 v79, v79, v53
	v_add_f32_e32 v78, v78, v54
	v_add_f32_e32 v79, v79, v55
	v_add_f32_e32 v78, v78, v79
	v_cvt_f64_f32_e32 v[84:85], v78
	v_cndmask_b32_e64 v75, v75, v80, s[20:21]
	v_mov_b32_e32 v73, v77
	v_add_f64 v[86:87], v[86:87], v[84:85]
	s_waitcnt vmcnt(9)
	v_max3_f32 v76, v56, v57, v58
	v_max3_f32 v76, v76, v59, v60
	v_max3_f32 v76, v76, v61, v62
	v_max_f32_e32 v76, v76, v63
	v_max_f32_e32 v77, v73, v76
	v_cmp_gt_f32_e64 s[20:21], v76, v73
	v_sub_f32_e32 v83, v73, v77
	v_mul_f32_e32 v83, s14, v83
	v_exp_f32_e32 v83, v83
	v_sub_f32_e32 v56, v56, v77
	v_sub_f32_e32 v57, v57, v77
	v_sub_f32_e32 v58, v58, v77
	v_sub_f32_e32 v59, v59, v77
	v_sub_f32_e32 v60, v60, v77
	v_sub_f32_e32 v61, v61, v77
	v_sub_f32_e32 v62, v62, v77
	v_sub_f32_e32 v63, v63, v77
	v_cvt_f64_f32_e32 v[84:85], v83
	v_or_b32_e32 v81, 48, v56
	v_or_b32_e32 v82, 49, v57
	v_min_u32_e32 v80, v81, v82
	v_or_b32_e32 v81, 50, v58
	v_or_b32_e32 v82, 51, v59
	v_min3_u32 v80, v80, v81, v82
	v_or_b32_e32 v81, 52, v60
	v_or_b32_e32 v82, 53, v61
	v_min3_u32 v80, v80, v81, v82
	v_or_b32_e32 v81, 54, v62
	v_or_b32_e32 v82, 55, v63
	v_min3_u32 v80, v80, v81, v82
	v_mul_f64 v[86:87], v[86:87], v[84:85]
	v_mul_f32_e32 v56, s14, v56
	v_mul_f32_e32 v57, s14, v57
	v_mul_f32_e32 v58, s14, v58
	v_mul_f32_e32 v59, s14, v59
	v_mul_f32_e32 v60, s14, v60
	v_mul_f32_e32 v61, s14, v61
	v_mul_f32_e32 v62, s14, v62
	v_mul_f32_e32 v63, s14, v63
	v_exp_f32_e32 v56, v56
	v_exp_f32_e32 v57, v57
	v_exp_f32_e32 v58, v58
	v_exp_f32_e32 v59, v59
	v_exp_f32_e32 v60, v60
	v_exp_f32_e32 v61, v61
	v_exp_f32_e32 v62, v62
	v_exp_f32_e32 v63, v63
	v_add_f32_e32 v78, v56, v58
	v_add_f32_e32 v79, v57, v59
	v_add_f32_e32 v78, v78, v60
	v_add_f32_e32 v79, v79, v61
	v_add_f32_e32 v78, v78, v62
	v_add_f32_e32 v79, v79, v63
	v_add_f32_e32 v78, v78, v79
	v_cvt_f64_f32_e32 v[84:85], v78
	v_cndmask_b32_e64 v75, v75, v80, s[20:21]
	v_mov_b32_e32 v73, v77
	v_add_f64 v[86:87], v[86:87], v[84:85]
	s_waitcnt vmcnt(4)
	v_max3_f32 v76, v64, v65, v66
	v_max3_f32 v76, v76, v67, v68
	v_max_f32_e32 v77, v73, v76
	v_cmp_gt_f32_e64 s[20:21], v76, v73
	v_sub_f32_e32 v83, v73, v77
	v_mul_f32_e32 v83, s14, v83
	v_exp_f32_e32 v83, v83
	v_sub_f32_e32 v64, v64, v77
	v_sub_f32_e32 v65, v65, v77
	v_sub_f32_e32 v66, v66, v77
	v_sub_f32_e32 v67, v67, v77
	v_sub_f32_e32 v68, v68, v77
	v_cvt_f64_f32_e32 v[84:85], v83
	v_or_b32_e32 v81, 56, v64
	v_or_b32_e32 v82, 57, v65
	v_min_u32_e32 v80, v81, v82
	v_or_b32_e32 v81, 58, v66
	v_or_b32_e32 v82, 59, v67
	v_min3_u32 v80, v80, v81, v82
	v_or_b32_e32 v81, 60, v68
	v_min_u32_e32 v80, v80, v81
	v_mul_f64 v[86:87], v[86:87], v[84:85]
	v_mul_f32_e32 v64, s14, v64
	v_mul_f32_e32 v65, s14, v65
	v_mul_f32_e32 v66, s14, v66
	v_mul_f32_e32 v67, s14, v67
	v_mul_f32_e32 v68, s14, v68
	v_exp_f32_e32 v64, v64
	v_exp_f32_e32 v65, v65
	v_exp_f32_e32 v66, v66
	v_exp_f32_e32 v67, v67
	v_exp_f32_e32 v68, v68
	v_add_f32_e32 v78, v64, v66
	v_add_f32_e32 v79, v65, v67
	v_add_f32_e32 v78, v78, v68
	v_add_f32_e32 v78, v78, v79
	v_cvt_f64_f32_e32 v[84:85], v78
	v_cndmask_b32_e64 v75, v75, v80, s[20:21]
	v_mov_b32_e32 v73, v77
	v_add_f64 v[86:87], v[86:87], v[84:85]
	s_waitcnt vmcnt(1)
	v_max3_f32 v76, v69, v70, v71
	v_max_f32_e32 v77, v73, v76
	v_cmp_gt_f32_e64 s[20:21], v76, v73
	v_sub_f32_e32 v83, v73, v77
	v_mul_f32_e32 v83, s14, v83
	v_exp_f32_e32 v83, v83
	v_sub_f32_e32 v69, v69, v77
	v_sub_f32_e32 v70, v70, v77
	v_sub_f32_e32 v71, v71, v77
	v_cvt_f64_f32_e32 v[84:85], v83
	v_or_b32_e32 v81, 61, v69
	v_or_b32_e32 v82, 62, v70
	v_min_u32_e32 v80, v81, v82
	v_or_b32_e32 v81, 63, v71
	v_min_u32_e32 v80, v80, v81
	v_mul_f64 v[86:87], v[86:87], v[84:85]
	v_mul_f32_e32 v69, s14, v69
	v_mul_f32_e32 v70, s14, v70
	v_mul_f32_e32 v71, s14, v71
	v_exp_f32_e32 v69, v69
	v_exp_f32_e32 v70, v70
	v_exp_f32_e32 v71, v71
	v_add_f32_e32 v78, v69, v70
	v_add_f32_e32 v78, v78, v71
	v_cvt_f64_f32_e32 v[84:85], v78
	v_cndmask_b32_e64 v75, v75, v80, s[20:21]
	v_mov_b32_e32 v73, v77
	v_add_f64 v[86:87], v[86:87], v[84:85]
	s_waitcnt vmcnt(0)
	v_max_f32_e32 v77, v73, v72
	v_cmp_gt_f32_e64 s[20:21], v72, v73
	v_sub_f32_e32 v83, v73, v77
	v_sub_f32_e32 v72, v72, v77
	v_mul_f32_e32 v83, s14, v83
	v_mul_f32_e32 v72, s14, v72
	v_exp_f32_e32 v83, v83
	v_exp_f32_e32 v72, v72
	v_cndmask_b32_e64 v75, v75, 64, s[20:21]
	v_cvt_f64_f32_e32 v[84:85], v83
	v_cvt_f64_f32_e32 v[90:91], v72
	v_mul_f64 v[86:87], v[86:87], v[84:85]
	v_add_f64 v[86:87], v[86:87], v[90:91]
	v_rcp_f64_e32 v[88:89], v[86:87]
	v_cmp_gt_u32_e32 vcc, 64, v75
	s_and_b64 vcc, vcc, s[36:37]
	v_fma_f64 v[90:91], -v[86:87], v[88:89], 1.0
	v_fma_f64 v[88:89], v[90:91], v[88:89], v[88:89]
	v_cvt_f32_f64_e32 v3, v[88:89]
	v_cndmask_b32_e32 v74, 0, v3, vcc
	global_store_dwordx2 v98, v[74:75], s[6:7]
